# v76 + phase H idle-time weight conversion claims 192 items per idle workgroup instead of 144
# speedup vs baseline: 1.0029x; 1.0029x over previous
.LBB0_4033:
	v_readlane_b32 s2, v254, 0
	v_readlane_b32 s3, v254, 1
	s_load_dword s0, s[2:3], 0x128
	v_readlane_b32 s4, v254, 50
	s_add_i32 s24, s4, 8
	s_waitcnt lgkmcnt(0)
	s_cmp_le_i32 s0, s24
	s_cbranch_scc0 .LBB0_4887
	s_load_dword s0, s[2:3], 0x12c
	s_waitcnt lgkmcnt(0)
	s_cmp_ge_i32 s24, s0
	s_cbranch_scc1 .LBB0_4887
	v_readlane_b32 s10, v254, 0
	v_readlane_b32 s11, v254, 1
	s_load_dwordx2 s[8:9], s[10:11], 0x120
	s_mov_b32 s25, s43
	s_cmpk_gt_i32 s25, 0x9f
	v_readlane_b32 s4, v254, 31
	s_cselect_b64 s[2:3], -1, 0
	v_readlane_b32 s5, v254, 32
	s_and_b64 s[2:3], s[4:5], s[2:3]
	s_waitcnt vmcnt(0)
	v_mov_b32_e32 v161, v235
	v_readlane_b32 s26, v254, 6
	s_andn2_b64 vcc, exec, s[2:3]
	s_cbranch_vccnz .LBB0_4850
	v_cmp_eq_u32_e32 vcc, 0, v161
	s_and_saveexec_b64 s[2:3], vcc
	s_cbranch_execz .LBB0_4040
	s_mov_b64 s[6:7], exec
	v_mbcnt_lo_u32_b32 v0, s6, 0
	v_mbcnt_hi_u32_b32 v0, s7, v0
	v_cmp_eq_u32_e32 vcc, 0, v0
	s_and_saveexec_b64 s[4:5], vcc
	s_cbranch_execz .LBB0_4039
	s_bcnt1_i32_b64 s0, s[6:7]
	s_mulk_i32 s0, 0xc0
	v_mov_b32_e32 v2, s0
	v_mov_b32_e32 v3, 0x38000
	s_waitcnt lgkmcnt(0)
	global_atomic_add v2, v3, v2, s[8:9] sc0
.LBB0_4039:
	s_or_b64 exec, exec, s[4:5]
	s_waitcnt vmcnt(0)
	v_readfirstlane_b32 s0, v2
	s_nop 1
	v_mov_b32_e32 v2, s0
	s_movk_i32 s0, 0xc0
	v_mad_u32_u24 v0, v0, s0, v2
	v_readlane_b32 s0, v254, 28
	s_nop 1
	v_mov_b32_e32 v2, s0
	ds_write_b32 v2, v0
.LBB0_4040:
	s_or_b64 exec, exec, s[2:3]
	v_readlane_b32 s0, v254, 28
	s_waitcnt lgkmcnt(0)
	s_barrier
	v_mov_b32_e32 v0, s0
	ds_read_b32 v0, v0
	s_waitcnt lgkmcnt(0)
	s_barrier
	v_readfirstlane_b32 s27, v0
	s_cmp_gt_i32 s27, 0xbfff
	s_cbranch_scc1 .LBB0_4850
	s_min_i32 s16, s27, 0xbf40
	s_addk_i32 s16, 0xc0
	s_add_i32 s27, s27, s26
	s_cmp_ge_i32 s27, s16
	s_cbranch_scc1 .LBB0_4850
	s_mul_hi_i32 s0, s27, 0x2aaaaaab
	s_lshr_b32 s2, s0, 31
	s_ashr_i32 s0, s0, 9
	s_add_i32 s2, s0, s2
	s_mul_i32 s0, s2, 0xc00
	s_sub_i32 s0, s27, s0
	s_cmpk_gt_i32 s0, 0x7ff
	s_mov_b64 s[6:7], -1
	s_cbranch_scc0 .LBB0_4044
	s_load_dwordx2 s[4:5], s[10:11], 0x108
	s_and_b32 s6, s0, 0x7fffffc0
	s_ashr_i32 s3, s2, 31
	s_add_i32 s92, s6, 0xfffff800
	s_lshl_b64 s[6:7], s[2:3], 23
	s_waitcnt lgkmcnt(0)
	s_add_u32 s3, s4, s6
	s_addc_u32 s6, s5, s7
	s_lshl_b64 s[4:5], s[92:93], 13
	s_add_u32 s3, s3, s4
	s_addc_u32 s4, s6, s5
	s_lshl_b32 s5, s0, 7
	s_and_b32 s5, s5, 0x1f80
	s_add_u32 s3, s3, s5
	s_addc_u32 s5, s4, 0
	s_add_u32 s4, s3, 0x8000000
	s_addc_u32 s5, s5, 0
	s_mov_b64 s[6:7], 0
